# GLU gate epilogue rewritten by hand: bias loaded once, 16 aux loads in flight, packed f32 sigmoid, counted vmcnt
# speedup vs baseline: 1.0700x; 1.0014x over previous
.LBB0_588:
	s_add_u32 s10, s13, 0x197cb600
	s_addc_u32 s11, s12, 0
	s_mul_hi_i32 s0, s16, 0x700
	s_mulk_i32 s16, 0x700
	s_add_u32 s8, s15, s16
	s_addc_u32 s9, s14, s0
	s_add_u32 s12, s18, 0x4cb9fd00
	s_mov_b32 s0, s37
	s_mov_b32 s1, s33
	s_addc_u32 s13, s17, 0
	s_lshl_b32 s2, s1, 4
	v_mbcnt_lo_u32_b32 v128, -1, s0
	s_lshl_b32 s0, s22, 8
	s_andn2_b32 s2, s2, 63
	v_mbcnt_hi_u32_b32 v128, -1, v128
	s_add_i32 s2, s2, s0
	s_lshl_b32 s1, s1, 5
	v_and_or_b32 v130, v128, 15, s2
	s_lshl_b32 s0, s21, 8
	s_and_b32 s1, s1, 0x60
	v_ashrrev_i32_e32 v128, 2, v128
	s_or_b32 s0, s1, s0
	v_and_b32_e32 v128, -4, v128
	v_ashrrev_i32_e32 v131, 31, v130
	v_add_u32_e32 v128, s0, v128
	s_movk_i32 s0, 0x1c0
	v_lshlrev_b64 v[132:133], 12, v[130:131]
	v_cmp_gt_i32_e32 vcc, s0, v128
	v_ashrrev_i32_e32 v129, 31, v128
	v_lshl_add_u64 v[132:133], s[12:13], 0, v[132:133]
	s_mov_b64 s[30:31], exec
	s_movk_i32 s2, 0x1c0
	v_cmp_gt_i32_e64 s[0:1], s2, v128
	s_movk_i32 s2, 0x1b0
	v_cmp_gt_i32_e64 s[4:5], s2, v128
	s_movk_i32 s2, 0x140
	v_cmp_gt_i32_e64 s[6:7], s2, v128
	s_movk_i32 s2, 0x130
	v_cmp_gt_i32_e64 s[14:15], s2, v128
	v_lshlrev_b64 v[134:135], 2, v[128:129]
	v_lshl_add_u64 v[136:137], s[8:9], 0, v[134:135]
	v_mov_b64_e32 v[138:139], s[10:11]
	v_mad_i64_i32 v[138:139], s[22:23], v130, s95, v[138:139]
	v_lshl_add_u64 v[138:139], v[138:139], 0, v[134:135]
	v_lshl_add_u64 v[140:141], v[128:129], 1, v[132:133]
	s_mov_b32 s16, 0xbfb8aa3b
	s_mov_b32 s17, 0xbfb8aa3b
	s_mov_b32 s18, 1.0
	s_mov_b32 s19, 1.0
	s_mov_b32 s22, 0x7000
	s_mov_b32 s23, 0
	s_mov_b32 s24, 0x23000
	s_mov_b32 s25, 0
	s_mov_b32 s26, 0x10000
	s_mov_b32 s27, 0
	s_mov_b32 s28, 0x50000
	s_mov_b32 s29, 0
	s_mov_b64 exec, s[0:1]
	global_load_dwordx4 v[146:149], v[136:137], off
	s_mov_b64 exec, s[4:5]
	global_load_dwordx4 v[150:153], v[136:137], off offset:64
	s_mov_b64 exec, s[6:7]
	global_load_dwordx4 v[154:157], v[136:137], off offset:512
	s_mov_b64 exec, s[14:15]
	global_load_dwordx4 v[158:161], v[136:137], off offset:576
	s_mov_b64 exec, s[0:1]
	global_load_dwordx4 v[162:165], v[138:139], off
	s_mov_b64 exec, s[4:5]
	global_load_dwordx4 v[166:169], v[138:139], off offset:64
	s_mov_b64 exec, s[6:7]
	global_load_dwordx4 v[170:173], v[138:139], off offset:512
	s_mov_b64 exec, s[14:15]
	global_load_dwordx4 v[174:177], v[138:139], off offset:576
	s_mov_b64 exec, s[30:31]
	v_lshl_add_u64 v[138:139], s[22:23], 0, v[138:139]
	s_mov_b64 exec, s[0:1]
	global_load_dwordx4 v[178:181], v[138:139], off
	s_mov_b64 exec, s[4:5]
	global_load_dwordx4 v[182:185], v[138:139], off offset:64
	s_mov_b64 exec, s[6:7]
	global_load_dwordx4 v[186:189], v[138:139], off offset:512
	s_mov_b64 exec, s[14:15]
	global_load_dwordx4 v[206:209], v[138:139], off offset:576
	s_mov_b64 exec, s[30:31]
	v_lshl_add_u64 v[138:139], s[22:23], 0, v[138:139]
	s_mov_b64 exec, s[0:1]
	global_load_dwordx4 v[210:213], v[138:139], off
	s_mov_b64 exec, s[4:5]
	global_load_dwordx4 v[214:217], v[138:139], off offset:64
	s_mov_b64 exec, s[6:7]
	global_load_dwordx4 v[224:227], v[138:139], off offset:512
	s_mov_b64 exec, s[14:15]
	global_load_dwordx4 v[228:231], v[138:139], off offset:576
	s_mov_b64 exec, s[30:31]
	v_lshl_add_u64 v[138:139], s[22:23], 0, v[138:139]
	s_mov_b64 exec, s[0:1]
	global_load_dwordx4 v[232:235], v[138:139], off
	s_mov_b64 exec, s[4:5]
	global_load_dwordx4 v[236:239], v[138:139], off offset:64
	s_mov_b64 exec, s[6:7]
	global_load_dwordx4 v[240:243], v[138:139], off offset:512
	s_mov_b64 exec, s[14:15]
	global_load_dwordx4 v[244:247], v[138:139], off offset:576
	s_mov_b64 exec, s[30:31]
	v_lshl_add_u64 v[138:139], s[24:25], 0, v[138:139]
	s_waitcnt vmcnt(16)
	v_pk_add_f32 v[124:125], v[124:125], v[146:147]
	v_pk_add_f32 v[126:127], v[126:127], v[148:149]
	v_pk_mul_f32 v[124:125], v[124:125], s[16:17]
	v_pk_mul_f32 v[126:127], v[126:127], s[16:17]
	v_exp_f32_e32 v124, v124
	v_exp_f32_e32 v125, v125
	v_exp_f32_e32 v126, v126
	v_exp_f32_e32 v127, v127
	v_pk_add_f32 v[124:125], v[124:125], s[18:19]
	v_pk_add_f32 v[126:127], v[126:127], s[18:19]
	v_rcp_f32_e32 v124, v124
	v_rcp_f32_e32 v125, v125
	v_rcp_f32_e32 v126, v126
	v_rcp_f32_e32 v127, v127
	v_pk_add_f32 v[120:121], v[120:121], v[150:151]
	v_pk_add_f32 v[122:123], v[122:123], v[152:153]
	v_pk_mul_f32 v[120:121], v[120:121], s[16:17]
	v_pk_mul_f32 v[122:123], v[122:123], s[16:17]
	v_exp_f32_e32 v120, v120
	v_exp_f32_e32 v121, v121
	v_exp_f32_e32 v122, v122
	v_exp_f32_e32 v123, v123
	v_pk_add_f32 v[120:121], v[120:121], s[18:19]
	v_pk_add_f32 v[122:123], v[122:123], s[18:19]
	v_rcp_f32_e32 v120, v120
	v_rcp_f32_e32 v121, v121
	v_rcp_f32_e32 v122, v122
	v_rcp_f32_e32 v123, v123
	v_pk_add_f32 v[116:117], v[116:117], v[154:155]
	v_pk_add_f32 v[118:119], v[118:119], v[156:157]
	v_pk_mul_f32 v[116:117], v[116:117], s[16:17]
	v_pk_mul_f32 v[118:119], v[118:119], s[16:17]
	v_exp_f32_e32 v116, v116
	v_exp_f32_e32 v117, v117
	v_exp_f32_e32 v118, v118
	v_exp_f32_e32 v119, v119
	v_pk_add_f32 v[116:117], v[116:117], s[18:19]
	v_pk_add_f32 v[118:119], v[118:119], s[18:19]
	v_rcp_f32_e32 v116, v116
	v_rcp_f32_e32 v117, v117
	v_rcp_f32_e32 v118, v118
	v_rcp_f32_e32 v119, v119
	v_pk_add_f32 v[112:113], v[112:113], v[158:159]
	v_pk_add_f32 v[114:115], v[114:115], v[160:161]
	v_pk_mul_f32 v[112:113], v[112:113], s[16:17]
	v_pk_mul_f32 v[114:115], v[114:115], s[16:17]
	v_exp_f32_e32 v112, v112
	v_exp_f32_e32 v113, v113
	v_exp_f32_e32 v114, v114
	v_exp_f32_e32 v115, v115
	v_pk_add_f32 v[112:113], v[112:113], s[18:19]
	v_pk_add_f32 v[114:115], v[114:115], s[18:19]
	v_rcp_f32_e32 v112, v112
	v_rcp_f32_e32 v113, v113
	v_rcp_f32_e32 v114, v114
	v_rcp_f32_e32 v115, v115
	v_pk_add_f32 v[108:109], v[108:109], v[146:147]
	v_pk_add_f32 v[110:111], v[110:111], v[148:149]
	v_pk_mul_f32 v[108:109], v[108:109], s[16:17]
	v_pk_mul_f32 v[110:111], v[110:111], s[16:17]
	v_exp_f32_e32 v108, v108
	v_exp_f32_e32 v109, v109
	v_exp_f32_e32 v110, v110
	v_exp_f32_e32 v111, v111
	v_pk_add_f32 v[108:109], v[108:109], s[18:19]
	v_pk_add_f32 v[110:111], v[110:111], s[18:19]
	v_rcp_f32_e32 v108, v108
	v_rcp_f32_e32 v109, v109
	v_rcp_f32_e32 v110, v110
	v_rcp_f32_e32 v111, v111
	v_pk_add_f32 v[104:105], v[104:105], v[150:151]
	v_pk_add_f32 v[106:107], v[106:107], v[152:153]
	v_pk_mul_f32 v[104:105], v[104:105], s[16:17]
	v_pk_mul_f32 v[106:107], v[106:107], s[16:17]
	v_exp_f32_e32 v104, v104
	v_exp_f32_e32 v105, v105
	v_exp_f32_e32 v106, v106
	v_exp_f32_e32 v107, v107
	v_pk_add_f32 v[104:105], v[104:105], s[18:19]
	v_pk_add_f32 v[106:107], v[106:107], s[18:19]
	v_rcp_f32_e32 v104, v104
	v_rcp_f32_e32 v105, v105
	v_rcp_f32_e32 v106, v106
	v_rcp_f32_e32 v107, v107
	v_pk_add_f32 v[100:101], v[100:101], v[154:155]
	v_pk_add_f32 v[102:103], v[102:103], v[156:157]
	v_pk_mul_f32 v[100:101], v[100:101], s[16:17]
	v_pk_mul_f32 v[102:103], v[102:103], s[16:17]
	v_exp_f32_e32 v100, v100
	v_exp_f32_e32 v101, v101
	v_exp_f32_e32 v102, v102
	v_exp_f32_e32 v103, v103
	v_pk_add_f32 v[100:101], v[100:101], s[18:19]
	v_pk_add_f32 v[102:103], v[102:103], s[18:19]
	v_rcp_f32_e32 v100, v100
	v_rcp_f32_e32 v101, v101
	v_rcp_f32_e32 v102, v102
	v_rcp_f32_e32 v103, v103
	v_pk_add_f32 v[96:97], v[96:97], v[158:159]
	v_pk_add_f32 v[98:99], v[98:99], v[160:161]
	v_pk_mul_f32 v[96:97], v[96:97], s[16:17]
	v_pk_mul_f32 v[98:99], v[98:99], s[16:17]
	v_exp_f32_e32 v96, v96
	v_exp_f32_e32 v97, v97
	v_exp_f32_e32 v98, v98
	v_exp_f32_e32 v99, v99
	v_pk_add_f32 v[96:97], v[96:97], s[18:19]
	v_pk_add_f32 v[98:99], v[98:99], s[18:19]
	v_rcp_f32_e32 v96, v96
	v_rcp_f32_e32 v97, v97
	v_rcp_f32_e32 v98, v98
	v_rcp_f32_e32 v99, v99
	v_pk_add_f32 v[92:93], v[92:93], v[146:147]
	v_pk_add_f32 v[94:95], v[94:95], v[148:149]
	v_pk_mul_f32 v[92:93], v[92:93], s[16:17]
	v_pk_mul_f32 v[94:95], v[94:95], s[16:17]
	v_exp_f32_e32 v92, v92
	v_exp_f32_e32 v93, v93
	v_exp_f32_e32 v94, v94
	v_exp_f32_e32 v95, v95
	v_pk_add_f32 v[92:93], v[92:93], s[18:19]
	v_pk_add_f32 v[94:95], v[94:95], s[18:19]
	v_rcp_f32_e32 v92, v92
	v_rcp_f32_e32 v93, v93
	v_rcp_f32_e32 v94, v94
	v_rcp_f32_e32 v95, v95
	v_pk_add_f32 v[88:89], v[88:89], v[150:151]
	v_pk_add_f32 v[90:91], v[90:91], v[152:153]
	v_pk_mul_f32 v[88:89], v[88:89], s[16:17]
	v_pk_mul_f32 v[90:91], v[90:91], s[16:17]
	v_exp_f32_e32 v88, v88
	v_exp_f32_e32 v89, v89
	v_exp_f32_e32 v90, v90
	v_exp_f32_e32 v91, v91
	v_pk_add_f32 v[88:89], v[88:89], s[18:19]
	v_pk_add_f32 v[90:91], v[90:91], s[18:19]
	v_rcp_f32_e32 v88, v88
	v_rcp_f32_e32 v89, v89
	v_rcp_f32_e32 v90, v90
	v_rcp_f32_e32 v91, v91
	v_pk_add_f32 v[84:85], v[84:85], v[154:155]
	v_pk_add_f32 v[86:87], v[86:87], v[156:157]
	v_pk_mul_f32 v[84:85], v[84:85], s[16:17]
	v_pk_mul_f32 v[86:87], v[86:87], s[16:17]
	v_exp_f32_e32 v84, v84
	v_exp_f32_e32 v85, v85
	v_exp_f32_e32 v86, v86
	v_exp_f32_e32 v87, v87
	v_pk_add_f32 v[84:85], v[84:85], s[18:19]
	v_pk_add_f32 v[86:87], v[86:87], s[18:19]
	v_rcp_f32_e32 v84, v84
	v_rcp_f32_e32 v85, v85
	v_rcp_f32_e32 v86, v86
	v_rcp_f32_e32 v87, v87
	v_pk_add_f32 v[80:81], v[80:81], v[158:159]
	v_pk_add_f32 v[82:83], v[82:83], v[160:161]
	v_pk_mul_f32 v[80:81], v[80:81], s[16:17]
	v_pk_mul_f32 v[82:83], v[82:83], s[16:17]
	v_exp_f32_e32 v80, v80
	v_exp_f32_e32 v81, v81
	v_exp_f32_e32 v82, v82
	v_exp_f32_e32 v83, v83
	v_pk_add_f32 v[80:81], v[80:81], s[18:19]
	v_pk_add_f32 v[82:83], v[82:83], s[18:19]
	v_rcp_f32_e32 v80, v80
	v_rcp_f32_e32 v81, v81
	v_rcp_f32_e32 v82, v82
	v_rcp_f32_e32 v83, v83
	v_pk_add_f32 v[76:77], v[76:77], v[146:147]
	v_pk_add_f32 v[78:79], v[78:79], v[148:149]
	v_pk_mul_f32 v[76:77], v[76:77], s[16:17]
	v_pk_mul_f32 v[78:79], v[78:79], s[16:17]
	v_exp_f32_e32 v76, v76
	v_exp_f32_e32 v77, v77
	v_exp_f32_e32 v78, v78
	v_exp_f32_e32 v79, v79
	v_pk_add_f32 v[76:77], v[76:77], s[18:19]
	v_pk_add_f32 v[78:79], v[78:79], s[18:19]
	v_rcp_f32_e32 v76, v76
	v_rcp_f32_e32 v77, v77
	v_rcp_f32_e32 v78, v78
	v_rcp_f32_e32 v79, v79
	v_pk_add_f32 v[72:73], v[72:73], v[150:151]
	v_pk_add_f32 v[74:75], v[74:75], v[152:153]
	v_pk_mul_f32 v[72:73], v[72:73], s[16:17]
	v_pk_mul_f32 v[74:75], v[74:75], s[16:17]
	v_exp_f32_e32 v72, v72
	v_exp_f32_e32 v73, v73
	v_exp_f32_e32 v74, v74
	v_exp_f32_e32 v75, v75
	v_pk_add_f32 v[72:73], v[72:73], s[18:19]
	v_pk_add_f32 v[74:75], v[74:75], s[18:19]
	v_rcp_f32_e32 v72, v72
	v_rcp_f32_e32 v73, v73
	v_rcp_f32_e32 v74, v74
	v_rcp_f32_e32 v75, v75
	v_pk_add_f32 v[68:69], v[68:69], v[154:155]
	v_pk_add_f32 v[70:71], v[70:71], v[156:157]
	v_pk_mul_f32 v[68:69], v[68:69], s[16:17]
	v_pk_mul_f32 v[70:71], v[70:71], s[16:17]
	v_exp_f32_e32 v68, v68
	v_exp_f32_e32 v69, v69
	v_exp_f32_e32 v70, v70
	v_exp_f32_e32 v71, v71
	v_pk_add_f32 v[68:69], v[68:69], s[18:19]
	v_pk_add_f32 v[70:71], v[70:71], s[18:19]
	v_rcp_f32_e32 v68, v68
	v_rcp_f32_e32 v69, v69
	v_rcp_f32_e32 v70, v70
	v_rcp_f32_e32 v71, v71
	v_pk_add_f32 v[64:65], v[64:65], v[158:159]
	v_pk_add_f32 v[66:67], v[66:67], v[160:161]
	v_pk_mul_f32 v[64:65], v[64:65], s[16:17]
	v_pk_mul_f32 v[66:67], v[66:67], s[16:17]
	v_exp_f32_e32 v64, v64
	v_exp_f32_e32 v65, v65
	v_exp_f32_e32 v66, v66
	v_exp_f32_e32 v67, v67
	v_pk_add_f32 v[64:65], v[64:65], s[18:19]
	v_pk_add_f32 v[66:67], v[66:67], s[18:19]
	v_rcp_f32_e32 v64, v64
	v_rcp_f32_e32 v65, v65
	v_rcp_f32_e32 v66, v66
	v_rcp_f32_e32 v67, v67
	s_waitcnt vmcnt(12)
	v_pk_mul_f32 v[124:125], v[162:163], v[124:125]
	v_pk_mul_f32 v[126:127], v[164:165], v[126:127]
	v_pk_mul_f32 v[120:121], v[166:167], v[120:121]
	v_pk_mul_f32 v[122:123], v[168:169], v[122:123]
	v_pk_mul_f32 v[116:117], v[170:171], v[116:117]
	v_pk_mul_f32 v[118:119], v[172:173], v[118:119]
	v_pk_mul_f32 v[112:113], v[174:175], v[112:113]
	v_pk_mul_f32 v[114:115], v[176:177], v[114:115]
	v_cvt_pk_bf16_f32 v124, v124, v125
	v_cvt_pk_bf16_f32 v125, v126, v127
	v_cvt_pk_bf16_f32 v120, v120, v121
	v_cvt_pk_bf16_f32 v121, v122, v123
	v_cvt_pk_bf16_f32 v116, v116, v117
	v_cvt_pk_bf16_f32 v117, v118, v119
	v_cvt_pk_bf16_f32 v112, v112, v113
	v_cvt_pk_bf16_f32 v113, v114, v115
	s_mov_b64 exec, s[0:1]
	global_store_dwordx2 v[140:141], v[124:125], off offset:896
	global_load_dwordx4 v[162:165], v[138:139], off
	s_mov_b64 exec, s[4:5]
	global_store_dwordx2 v[140:141], v[120:121], off offset:928
	global_load_dwordx4 v[166:169], v[138:139], off offset:64
	s_mov_b64 exec, s[6:7]
	global_store_dwordx2 v[140:141], v[116:117], off offset:1152
	global_load_dwordx4 v[170:173], v[138:139], off offset:512
	s_mov_b64 exec, s[14:15]
	global_store_dwordx2 v[140:141], v[112:113], off offset:1184
	global_load_dwordx4 v[174:177], v[138:139], off offset:576
	s_mov_b64 exec, s[30:31]
	v_lshl_add_u64 v[140:141], s[26:27], 0, v[140:141]
	v_lshl_add_u64 v[138:139], s[22:23], 0, v[138:139]
	s_waitcnt vmcnt(16)
	v_pk_mul_f32 v[108:109], v[178:179], v[108:109]
	v_pk_mul_f32 v[110:111], v[180:181], v[110:111]
	v_pk_mul_f32 v[104:105], v[182:183], v[104:105]
	v_pk_mul_f32 v[106:107], v[184:185], v[106:107]
	v_pk_mul_f32 v[100:101], v[186:187], v[100:101]
	v_pk_mul_f32 v[102:103], v[188:189], v[102:103]
	v_pk_mul_f32 v[96:97], v[206:207], v[96:97]
	v_pk_mul_f32 v[98:99], v[208:209], v[98:99]
	v_cvt_pk_bf16_f32 v108, v108, v109
	v_cvt_pk_bf16_f32 v109, v110, v111
	v_cvt_pk_bf16_f32 v104, v104, v105
	v_cvt_pk_bf16_f32 v105, v106, v107
	v_cvt_pk_bf16_f32 v100, v100, v101
	v_cvt_pk_bf16_f32 v101, v102, v103
	v_cvt_pk_bf16_f32 v96, v96, v97
	v_cvt_pk_bf16_f32 v97, v98, v99
	s_mov_b64 exec, s[0:1]
	global_store_dwordx2 v[140:141], v[108:109], off offset:896
	global_load_dwordx4 v[178:181], v[138:139], off
	s_mov_b64 exec, s[4:5]
	global_store_dwordx2 v[140:141], v[104:105], off offset:928
	global_load_dwordx4 v[182:185], v[138:139], off offset:64
	s_mov_b64 exec, s[6:7]
	global_store_dwordx2 v[140:141], v[100:101], off offset:1152
	global_load_dwordx4 v[186:189], v[138:139], off offset:512
	s_mov_b64 exec, s[14:15]
	global_store_dwordx2 v[140:141], v[96:97], off offset:1184
	global_load_dwordx4 v[206:209], v[138:139], off offset:576
	s_mov_b64 exec, s[30:31]
	v_lshl_add_u64 v[140:141], s[26:27], 0, v[140:141]
	v_lshl_add_u64 v[138:139], s[22:23], 0, v[138:139]
	s_waitcnt vmcnt(20)
	v_pk_mul_f32 v[92:93], v[210:211], v[92:93]
	v_pk_mul_f32 v[94:95], v[212:213], v[94:95]
	v_pk_mul_f32 v[88:89], v[214:215], v[88:89]
	v_pk_mul_f32 v[90:91], v[216:217], v[90:91]
	v_pk_mul_f32 v[84:85], v[224:225], v[84:85]
	v_pk_mul_f32 v[86:87], v[226:227], v[86:87]
	v_pk_mul_f32 v[80:81], v[228:229], v[80:81]
	v_pk_mul_f32 v[82:83], v[230:231], v[82:83]
	v_cvt_pk_bf16_f32 v92, v92, v93
	v_cvt_pk_bf16_f32 v93, v94, v95
	v_cvt_pk_bf16_f32 v88, v88, v89
	v_cvt_pk_bf16_f32 v89, v90, v91
	v_cvt_pk_bf16_f32 v84, v84, v85
	v_cvt_pk_bf16_f32 v85, v86, v87
	v_cvt_pk_bf16_f32 v80, v80, v81
	v_cvt_pk_bf16_f32 v81, v82, v83
	s_mov_b64 exec, s[0:1]
	global_store_dwordx2 v[140:141], v[92:93], off offset:896
	global_load_dwordx4 v[210:213], v[138:139], off
	s_mov_b64 exec, s[4:5]
	global_store_dwordx2 v[140:141], v[88:89], off offset:928
	global_load_dwordx4 v[214:217], v[138:139], off offset:64
	s_mov_b64 exec, s[6:7]
	global_store_dwordx2 v[140:141], v[84:85], off offset:1152
	global_load_dwordx4 v[224:227], v[138:139], off offset:512
	s_mov_b64 exec, s[14:15]
	global_store_dwordx2 v[140:141], v[80:81], off offset:1184
	global_load_dwordx4 v[228:231], v[138:139], off offset:576
	s_mov_b64 exec, s[30:31]
	v_lshl_add_u64 v[140:141], s[26:27], 0, v[140:141]
	v_lshl_add_u64 v[138:139], s[22:23], 0, v[138:139]
	s_waitcnt vmcnt(24)
	v_pk_mul_f32 v[76:77], v[232:233], v[76:77]
	v_pk_mul_f32 v[78:79], v[234:235], v[78:79]
	v_pk_mul_f32 v[72:73], v[236:237], v[72:73]
	v_pk_mul_f32 v[74:75], v[238:239], v[74:75]
	v_pk_mul_f32 v[68:69], v[240:241], v[68:69]
	v_pk_mul_f32 v[70:71], v[242:243], v[70:71]
	v_pk_mul_f32 v[64:65], v[244:245], v[64:65]
	v_pk_mul_f32 v[66:67], v[246:247], v[66:67]
	v_cvt_pk_bf16_f32 v76, v76, v77
	v_cvt_pk_bf16_f32 v77, v78, v79
	v_cvt_pk_bf16_f32 v72, v72, v73
	v_cvt_pk_bf16_f32 v73, v74, v75
	v_cvt_pk_bf16_f32 v68, v68, v69
	v_cvt_pk_bf16_f32 v69, v70, v71
	v_cvt_pk_bf16_f32 v64, v64, v65
	v_cvt_pk_bf16_f32 v65, v66, v67
	s_mov_b64 exec, s[0:1]
	global_store_dwordx2 v[140:141], v[76:77], off offset:896
	global_load_dwordx4 v[232:235], v[138:139], off
	s_mov_b64 exec, s[4:5]
	global_store_dwordx2 v[140:141], v[72:73], off offset:928
	global_load_dwordx4 v[236:239], v[138:139], off offset:64
	s_mov_b64 exec, s[6:7]
	global_store_dwordx2 v[140:141], v[68:69], off offset:1152
	global_load_dwordx4 v[240:243], v[138:139], off offset:512
	s_mov_b64 exec, s[14:15]
	global_store_dwordx2 v[140:141], v[64:65], off offset:1184
	global_load_dwordx4 v[244:247], v[138:139], off offset:576
	s_mov_b64 exec, s[30:31]
	v_lshl_add_u64 v[140:141], s[28:29], 0, v[140:141]
	v_pk_add_f32 v[60:61], v[60:61], v[146:147]
	v_pk_add_f32 v[62:63], v[62:63], v[148:149]
	v_pk_mul_f32 v[60:61], v[60:61], s[16:17]
	v_pk_mul_f32 v[62:63], v[62:63], s[16:17]
	v_exp_f32_e32 v60, v60
	v_exp_f32_e32 v61, v61
	v_exp_f32_e32 v62, v62
	v_exp_f32_e32 v63, v63
	v_pk_add_f32 v[60:61], v[60:61], s[18:19]
	v_pk_add_f32 v[62:63], v[62:63], s[18:19]
	v_rcp_f32_e32 v60, v60
	v_rcp_f32_e32 v61, v61
	v_rcp_f32_e32 v62, v62
	v_rcp_f32_e32 v63, v63
	v_pk_add_f32 v[56:57], v[56:57], v[150:151]
	v_pk_add_f32 v[58:59], v[58:59], v[152:153]
	v_pk_mul_f32 v[56:57], v[56:57], s[16:17]
	v_pk_mul_f32 v[58:59], v[58:59], s[16:17]
	v_exp_f32_e32 v56, v56
	v_exp_f32_e32 v57, v57
	v_exp_f32_e32 v58, v58
	v_exp_f32_e32 v59, v59
	v_pk_add_f32 v[56:57], v[56:57], s[18:19]
	v_pk_add_f32 v[58:59], v[58:59], s[18:19]
	v_rcp_f32_e32 v56, v56
	v_rcp_f32_e32 v57, v57
	v_rcp_f32_e32 v58, v58
	v_rcp_f32_e32 v59, v59
	v_pk_add_f32 v[52:53], v[52:53], v[154:155]
	v_pk_add_f32 v[54:55], v[54:55], v[156:157]
	v_pk_mul_f32 v[52:53], v[52:53], s[16:17]
	v_pk_mul_f32 v[54:55], v[54:55], s[16:17]
	v_exp_f32_e32 v52, v52
	v_exp_f32_e32 v53, v53
	v_exp_f32_e32 v54, v54
	v_exp_f32_e32 v55, v55
	v_pk_add_f32 v[52:53], v[52:53], s[18:19]
	v_pk_add_f32 v[54:55], v[54:55], s[18:19]
	v_rcp_f32_e32 v52, v52
	v_rcp_f32_e32 v53, v53
	v_rcp_f32_e32 v54, v54
	v_rcp_f32_e32 v55, v55
	v_pk_add_f32 v[48:49], v[48:49], v[158:159]
	v_pk_add_f32 v[50:51], v[50:51], v[160:161]
	v_pk_mul_f32 v[48:49], v[48:49], s[16:17]
	v_pk_mul_f32 v[50:51], v[50:51], s[16:17]
	v_exp_f32_e32 v48, v48
	v_exp_f32_e32 v49, v49
	v_exp_f32_e32 v50, v50
	v_exp_f32_e32 v51, v51
	v_pk_add_f32 v[48:49], v[48:49], s[18:19]
	v_pk_add_f32 v[50:51], v[50:51], s[18:19]
	v_rcp_f32_e32 v48, v48
	v_rcp_f32_e32 v49, v49
	v_rcp_f32_e32 v50, v50
	v_rcp_f32_e32 v51, v51
	v_pk_add_f32 v[44:45], v[44:45], v[146:147]
	v_pk_add_f32 v[46:47], v[46:47], v[148:149]
	v_pk_mul_f32 v[44:45], v[44:45], s[16:17]
	v_pk_mul_f32 v[46:47], v[46:47], s[16:17]
	v_exp_f32_e32 v44, v44
	v_exp_f32_e32 v45, v45
	v_exp_f32_e32 v46, v46
	v_exp_f32_e32 v47, v47
	v_pk_add_f32 v[44:45], v[44:45], s[18:19]
	v_pk_add_f32 v[46:47], v[46:47], s[18:19]
	v_rcp_f32_e32 v44, v44
	v_rcp_f32_e32 v45, v45
	v_rcp_f32_e32 v46, v46
	v_rcp_f32_e32 v47, v47
	v_pk_add_f32 v[40:41], v[40:41], v[150:151]
	v_pk_add_f32 v[42:43], v[42:43], v[152:153]
	v_pk_mul_f32 v[40:41], v[40:41], s[16:17]
	v_pk_mul_f32 v[42:43], v[42:43], s[16:17]
	v_exp_f32_e32 v40, v40
	v_exp_f32_e32 v41, v41
	v_exp_f32_e32 v42, v42
	v_exp_f32_e32 v43, v43
	v_pk_add_f32 v[40:41], v[40:41], s[18:19]
	v_pk_add_f32 v[42:43], v[42:43], s[18:19]
	v_rcp_f32_e32 v40, v40
	v_rcp_f32_e32 v41, v41
	v_rcp_f32_e32 v42, v42
	v_rcp_f32_e32 v43, v43
	v_pk_add_f32 v[36:37], v[36:37], v[154:155]
	v_pk_add_f32 v[38:39], v[38:39], v[156:157]
	v_pk_mul_f32 v[36:37], v[36:37], s[16:17]
	v_pk_mul_f32 v[38:39], v[38:39], s[16:17]
	v_exp_f32_e32 v36, v36
	v_exp_f32_e32 v37, v37
	v_exp_f32_e32 v38, v38
	v_exp_f32_e32 v39, v39
	v_pk_add_f32 v[36:37], v[36:37], s[18:19]
	v_pk_add_f32 v[38:39], v[38:39], s[18:19]
	v_rcp_f32_e32 v36, v36
	v_rcp_f32_e32 v37, v37
	v_rcp_f32_e32 v38, v38
	v_rcp_f32_e32 v39, v39
	v_pk_add_f32 v[32:33], v[32:33], v[158:159]
	v_pk_add_f32 v[34:35], v[34:35], v[160:161]
	v_pk_mul_f32 v[32:33], v[32:33], s[16:17]
	v_pk_mul_f32 v[34:35], v[34:35], s[16:17]
	v_exp_f32_e32 v32, v32
	v_exp_f32_e32 v33, v33
	v_exp_f32_e32 v34, v34
	v_exp_f32_e32 v35, v35
	v_pk_add_f32 v[32:33], v[32:33], s[18:19]
	v_pk_add_f32 v[34:35], v[34:35], s[18:19]
	v_rcp_f32_e32 v32, v32
	v_rcp_f32_e32 v33, v33
	v_rcp_f32_e32 v34, v34
	v_rcp_f32_e32 v35, v35
	v_pk_add_f32 v[28:29], v[28:29], v[146:147]
	v_pk_add_f32 v[30:31], v[30:31], v[148:149]
	v_pk_mul_f32 v[28:29], v[28:29], s[16:17]
	v_pk_mul_f32 v[30:31], v[30:31], s[16:17]
	v_exp_f32_e32 v28, v28
	v_exp_f32_e32 v29, v29
	v_exp_f32_e32 v30, v30
	v_exp_f32_e32 v31, v31
	v_pk_add_f32 v[28:29], v[28:29], s[18:19]
	v_pk_add_f32 v[30:31], v[30:31], s[18:19]
	v_rcp_f32_e32 v28, v28
	v_rcp_f32_e32 v29, v29
	v_rcp_f32_e32 v30, v30
	v_rcp_f32_e32 v31, v31
	v_pk_add_f32 v[24:25], v[24:25], v[150:151]
	v_pk_add_f32 v[26:27], v[26:27], v[152:153]
	v_pk_mul_f32 v[24:25], v[24:25], s[16:17]
	v_pk_mul_f32 v[26:27], v[26:27], s[16:17]
	v_exp_f32_e32 v24, v24
	v_exp_f32_e32 v25, v25
	v_exp_f32_e32 v26, v26
	v_exp_f32_e32 v27, v27
	v_pk_add_f32 v[24:25], v[24:25], s[18:19]
	v_pk_add_f32 v[26:27], v[26:27], s[18:19]
	v_rcp_f32_e32 v24, v24
	v_rcp_f32_e32 v25, v25
	v_rcp_f32_e32 v26, v26
	v_rcp_f32_e32 v27, v27
	v_pk_add_f32 v[20:21], v[20:21], v[154:155]
	v_pk_add_f32 v[22:23], v[22:23], v[156:157]
	v_pk_mul_f32 v[20:21], v[20:21], s[16:17]
	v_pk_mul_f32 v[22:23], v[22:23], s[16:17]
	v_exp_f32_e32 v20, v20
	v_exp_f32_e32 v21, v21
	v_exp_f32_e32 v22, v22
	v_exp_f32_e32 v23, v23
	v_pk_add_f32 v[20:21], v[20:21], s[18:19]
	v_pk_add_f32 v[22:23], v[22:23], s[18:19]
	v_rcp_f32_e32 v20, v20
	v_rcp_f32_e32 v21, v21
	v_rcp_f32_e32 v22, v22
	v_rcp_f32_e32 v23, v23
	v_pk_add_f32 v[16:17], v[16:17], v[158:159]
	v_pk_add_f32 v[18:19], v[18:19], v[160:161]
	v_pk_mul_f32 v[16:17], v[16:17], s[16:17]
	v_pk_mul_f32 v[18:19], v[18:19], s[16:17]
	v_exp_f32_e32 v16, v16
	v_exp_f32_e32 v17, v17
	v_exp_f32_e32 v18, v18
	v_exp_f32_e32 v19, v19
	v_pk_add_f32 v[16:17], v[16:17], s[18:19]
	v_pk_add_f32 v[18:19], v[18:19], s[18:19]
	v_rcp_f32_e32 v16, v16
	v_rcp_f32_e32 v17, v17
	v_rcp_f32_e32 v18, v18
	v_rcp_f32_e32 v19, v19
	v_pk_add_f32 v[12:13], v[12:13], v[146:147]
	v_pk_add_f32 v[14:15], v[14:15], v[148:149]
	v_pk_mul_f32 v[12:13], v[12:13], s[16:17]
	v_pk_mul_f32 v[14:15], v[14:15], s[16:17]
	v_exp_f32_e32 v12, v12
	v_exp_f32_e32 v13, v13
	v_exp_f32_e32 v14, v14
	v_exp_f32_e32 v15, v15
	v_pk_add_f32 v[12:13], v[12:13], s[18:19]
	v_pk_add_f32 v[14:15], v[14:15], s[18:19]
	v_rcp_f32_e32 v12, v12
	v_rcp_f32_e32 v13, v13
	v_rcp_f32_e32 v14, v14
	v_rcp_f32_e32 v15, v15
	v_pk_add_f32 v[8:9], v[8:9], v[150:151]
	v_pk_add_f32 v[10:11], v[10:11], v[152:153]
	v_pk_mul_f32 v[8:9], v[8:9], s[16:17]
	v_pk_mul_f32 v[10:11], v[10:11], s[16:17]
	v_exp_f32_e32 v8, v8
	v_exp_f32_e32 v9, v9
	v_exp_f32_e32 v10, v10
	v_exp_f32_e32 v11, v11
	v_pk_add_f32 v[8:9], v[8:9], s[18:19]
	v_pk_add_f32 v[10:11], v[10:11], s[18:19]
	v_rcp_f32_e32 v8, v8
	v_rcp_f32_e32 v9, v9
	v_rcp_f32_e32 v10, v10
	v_rcp_f32_e32 v11, v11
	v_pk_add_f32 v[4:5], v[4:5], v[154:155]
	v_pk_add_f32 v[6:7], v[6:7], v[156:157]
	v_pk_mul_f32 v[4:5], v[4:5], s[16:17]
	v_pk_mul_f32 v[6:7], v[6:7], s[16:17]
	v_exp_f32_e32 v4, v4
	v_exp_f32_e32 v5, v5
	v_exp_f32_e32 v6, v6
	v_exp_f32_e32 v7, v7
	v_pk_add_f32 v[4:5], v[4:5], s[18:19]
	v_pk_add_f32 v[6:7], v[6:7], s[18:19]
	v_rcp_f32_e32 v4, v4
	v_rcp_f32_e32 v5, v5
	v_rcp_f32_e32 v6, v6
	v_rcp_f32_e32 v7, v7
	v_pk_add_f32 v[0:1], v[0:1], v[158:159]
	v_pk_add_f32 v[2:3], v[2:3], v[160:161]
	v_pk_mul_f32 v[0:1], v[0:1], s[16:17]
	v_pk_mul_f32 v[2:3], v[2:3], s[16:17]
	v_exp_f32_e32 v0, v0
	v_exp_f32_e32 v1, v1
	v_exp_f32_e32 v2, v2
	v_exp_f32_e32 v3, v3
	v_pk_add_f32 v[0:1], v[0:1], s[18:19]
	v_pk_add_f32 v[2:3], v[2:3], s[18:19]
	v_rcp_f32_e32 v0, v0
	v_rcp_f32_e32 v1, v1
	v_rcp_f32_e32 v2, v2
	v_rcp_f32_e32 v3, v3
	s_waitcnt vmcnt(24)
	v_pk_mul_f32 v[60:61], v[162:163], v[60:61]
	v_pk_mul_f32 v[62:63], v[164:165], v[62:63]
	v_pk_mul_f32 v[56:57], v[166:167], v[56:57]
	v_pk_mul_f32 v[58:59], v[168:169], v[58:59]
	v_pk_mul_f32 v[52:53], v[170:171], v[52:53]
	v_pk_mul_f32 v[54:55], v[172:173], v[54:55]
	v_pk_mul_f32 v[48:49], v[174:175], v[48:49]
	v_pk_mul_f32 v[50:51], v[176:177], v[50:51]
	v_cvt_pk_bf16_f32 v60, v60, v61
	v_cvt_pk_bf16_f32 v61, v62, v63
	v_cvt_pk_bf16_f32 v56, v56, v57
	v_cvt_pk_bf16_f32 v57, v58, v59
	v_cvt_pk_bf16_f32 v52, v52, v53
	v_cvt_pk_bf16_f32 v53, v54, v55
	v_cvt_pk_bf16_f32 v48, v48, v49
	v_cvt_pk_bf16_f32 v49, v50, v51
	s_mov_b64 exec, s[0:1]
	global_store_dwordx2 v[140:141], v[60:61], off offset:896
	s_mov_b64 exec, s[4:5]
	global_store_dwordx2 v[140:141], v[56:57], off offset:928
	s_mov_b64 exec, s[6:7]
	global_store_dwordx2 v[140:141], v[52:53], off offset:1152
	s_mov_b64 exec, s[14:15]
	global_store_dwordx2 v[140:141], v[48:49], off offset:1184
	s_mov_b64 exec, s[30:31]
	v_lshl_add_u64 v[140:141], s[26:27], 0, v[140:141]
	s_waitcnt vmcnt(20)
	v_pk_mul_f32 v[44:45], v[178:179], v[44:45]
	v_pk_mul_f32 v[46:47], v[180:181], v[46:47]
	v_pk_mul_f32 v[40:41], v[182:183], v[40:41]
	v_pk_mul_f32 v[42:43], v[184:185], v[42:43]
	v_pk_mul_f32 v[36:37], v[186:187], v[36:37]
	v_pk_mul_f32 v[38:39], v[188:189], v[38:39]
	v_pk_mul_f32 v[32:33], v[206:207], v[32:33]
	v_pk_mul_f32 v[34:35], v[208:209], v[34:35]
	v_cvt_pk_bf16_f32 v44, v44, v45
	v_cvt_pk_bf16_f32 v45, v46, v47
	v_cvt_pk_bf16_f32 v40, v40, v41
	v_cvt_pk_bf16_f32 v41, v42, v43
	v_cvt_pk_bf16_f32 v36, v36, v37
	v_cvt_pk_bf16_f32 v37, v38, v39
	v_cvt_pk_bf16_f32 v32, v32, v33
	v_cvt_pk_bf16_f32 v33, v34, v35
	s_mov_b64 exec, s[0:1]
	global_store_dwordx2 v[140:141], v[44:45], off offset:896
	s_mov_b64 exec, s[4:5]
	global_store_dwordx2 v[140:141], v[40:41], off offset:928
	s_mov_b64 exec, s[6:7]
	global_store_dwordx2 v[140:141], v[36:37], off offset:1152
	s_mov_b64 exec, s[14:15]
	global_store_dwordx2 v[140:141], v[32:33], off offset:1184
	s_mov_b64 exec, s[30:31]
	v_lshl_add_u64 v[140:141], s[26:27], 0, v[140:141]
	s_waitcnt vmcnt(16)
	v_pk_mul_f32 v[28:29], v[210:211], v[28:29]
	v_pk_mul_f32 v[30:31], v[212:213], v[30:31]
	v_pk_mul_f32 v[24:25], v[214:215], v[24:25]
	v_pk_mul_f32 v[26:27], v[216:217], v[26:27]
	v_pk_mul_f32 v[20:21], v[224:225], v[20:21]
	v_pk_mul_f32 v[22:23], v[226:227], v[22:23]
	v_pk_mul_f32 v[16:17], v[228:229], v[16:17]
	v_pk_mul_f32 v[18:19], v[230:231], v[18:19]
	v_cvt_pk_bf16_f32 v28, v28, v29
	v_cvt_pk_bf16_f32 v29, v30, v31
	v_cvt_pk_bf16_f32 v24, v24, v25
	v_cvt_pk_bf16_f32 v25, v26, v27
	v_cvt_pk_bf16_f32 v20, v20, v21
	v_cvt_pk_bf16_f32 v21, v22, v23
	v_cvt_pk_bf16_f32 v16, v16, v17
	v_cvt_pk_bf16_f32 v17, v18, v19
	s_mov_b64 exec, s[0:1]
	global_store_dwordx2 v[140:141], v[28:29], off offset:896
	s_mov_b64 exec, s[4:5]
	global_store_dwordx2 v[140:141], v[24:25], off offset:928
	s_mov_b64 exec, s[6:7]
	global_store_dwordx2 v[140:141], v[20:21], off offset:1152
	s_mov_b64 exec, s[14:15]
	global_store_dwordx2 v[140:141], v[16:17], off offset:1184
	s_mov_b64 exec, s[30:31]
	v_lshl_add_u64 v[140:141], s[26:27], 0, v[140:141]
	s_waitcnt vmcnt(12)
	v_pk_mul_f32 v[12:13], v[232:233], v[12:13]
	v_pk_mul_f32 v[14:15], v[234:235], v[14:15]
	v_pk_mul_f32 v[8:9], v[236:237], v[8:9]
	v_pk_mul_f32 v[10:11], v[238:239], v[10:11]
	v_pk_mul_f32 v[4:5], v[240:241], v[4:5]
	v_pk_mul_f32 v[6:7], v[242:243], v[6:7]
	v_pk_mul_f32 v[0:1], v[244:245], v[0:1]
	v_pk_mul_f32 v[2:3], v[246:247], v[2:3]
	v_cvt_pk_bf16_f32 v12, v12, v13
	v_cvt_pk_bf16_f32 v13, v14, v15
	v_cvt_pk_bf16_f32 v8, v8, v9
	v_cvt_pk_bf16_f32 v9, v10, v11
	v_cvt_pk_bf16_f32 v4, v4, v5
	v_cvt_pk_bf16_f32 v5, v6, v7
	v_cvt_pk_bf16_f32 v0, v0, v1
	v_cvt_pk_bf16_f32 v1, v2, v3
	s_mov_b64 exec, s[0:1]
	global_store_dwordx2 v[140:141], v[12:13], off offset:896
	s_mov_b64 exec, s[4:5]
	global_store_dwordx2 v[140:141], v[8:9], off offset:928
	s_mov_b64 exec, s[6:7]
	global_store_dwordx2 v[140:141], v[4:5], off offset:1152
	s_mov_b64 exec, s[14:15]
	global_store_dwordx2 v[140:141], v[0:1], off offset:1184
	s_mov_b64 exec, s[30:31]
	s_mov_b32 s20, 0x38e38e39
	s_mov_b32 s21, 0xe38e38e
.LBB0_652:
	s_waitcnt vmcnt(0)
	s_barrier
.LBB0_653:
	s_mov_b32 s0, s37
	s_mov_b32 s1, s33
	v_mbcnt_lo_u32_b32 v0, -1, s0
	v_mbcnt_hi_u32_b32 v0, -1, v0
	v_lshl_or_b32 v0, s1, 6, v0
	v_readlane_b32 s0, v254, 0
	v_readlane_b32 s1, v254, 1
	s_mov_b32 s1, s37
	s_add_i32 s1, s1, 0x20120
	v_mov_b32_e32 v1, s1
	ds_read_b64 v[2:3], v1
	s_mov_b32 s1, 0
	s_add_i32 s1, s1, 0x20120
	v_mov_b32_e32 v1, s1
	s_waitcnt lgkmcnt(0)
	v_readfirstlane_b32 s2, v3
	v_readfirstlane_b32 s4, v2
	ds_read_b64 v[2:3], v1
	s_mov_b32 s1, 0
	s_add_i32 s1, s1, 0x20120
	v_mov_b32_e32 v1, s1
	s_waitcnt lgkmcnt(0)
	v_readfirstlane_b32 s7, v3
	v_readfirstlane_b32 s6, v2
	ds_read_b64 v[2:3], v1
	s_ashr_i32 s1, s0, 31
	s_lshl_b64 s[0:1], s[0:1], 9
	v_ashrrev_i32_e32 v1, 31, v0
	v_lshl_add_u64 v[0:1], s[0:1], 0, v[0:1]
	s_mov_b64 s[0:1], 0x90000
	s_waitcnt lgkmcnt(0)
	v_readfirstlane_b32 s9, v3
	v_readfirstlane_b32 s8, v2
	v_cmp_gt_i64_e32 vcc, s[0:1], v[0:1]
	s_and_saveexec_b64 s[0:1], vcc
	s_cbranch_execz .LBB0_656
	s_add_u32 s4, s4, 0x18203600
	s_addc_u32 s5, s2, 0
	s_add_u32 s6, s6, 0x19403600
	s_addc_u32 s7, s7, 0
	s_add_u32 s8, s8, 0x4cb9fd00
	s_addc_u32 s9, s9, 0
	v_lshlrev_b32_e32 v2, 3, v0
	s_mov_b64 s[10:11], 0
